# NA q/k row RMS norm: 1/sqrt via one f32 v_rsq_f32 instead of the expanded IEEE sqrt+divide chain (33 dependent instr per row group)
# speedup vs baseline: 1.0850x; 1.0072x over previous
.LBB0_468:
	s_or_b64 exec, exec, s[4:5]
	s_ashr_i32 s94, s0, 9
	v_readlane_b32 s0, v252, 17
	s_add_i32 s92, s95, -4
	s_lshl_b32 s1, s86, 13
	v_or_b32_e32 v12, s0, v0
	v_readlane_b32 s0, v252, 24
	s_add_i32 s85, s86, s0
	s_lshl_b32 s0, s94, 3
	s_or_b32 s2, s0, s75
	s_ashr_i32 s3, s2, 31
	s_lshl_b32 s0, s86, 6
	s_lshl_b64 s[72:73], s[2:3], 21
	v_readlane_b32 s2, v252, 18
	s_add_u32 s2, s2, s72
	v_readlane_b32 s3, v252, 19
	s_addc_u32 s3, s3, s73
	s_add_u32 s2, s2, s1
	s_addc_u32 s3, s3, 0
	s_lshl_b64 s[96:97], s[92:93], 13
	s_add_u32 s1, s96, s72
	s_addc_u32 s4, s97, s73
	v_readlane_b32 s5, v252, 20
	s_add_u32 s6, s5, s1
	v_readlane_b32 s5, v252, 21
	s_addc_u32 s7, s5, s4
	v_readlane_b32 s5, v252, 22
	s_add_u32 s8, s5, s1
	v_readlane_b32 s1, v252, 23
	s_addc_u32 s9, s1, s4
	s_mov_b64 s[4:5], s[64:65]
	s_load_dwordx2 s[12:13], s[4:5], 0x28
	s_load_dwordx2 s[10:11], s[64:65], 0x30
	v_mbcnt_lo_u32_b32 v16, -1, 0
	v_mbcnt_hi_u32_b32 v16, -1, v16
	v_readlane_b32 s4, v252, 13
	v_and_b32_e32 v176, 31, v16
	v_ashrrev_i32_e32 v177, 5, v16
	v_or_b32_e32 v0, s4, v176
	v_lshlrev_b64 v[2:3], 7, v[0:1]
	v_lshl_add_u64 v[4:5], s[2:3], 0, v[2:3]
	v_lshlrev_b32_e32 v2, 3, v177
	v_ashrrev_i32_e32 v3, 31, v2
	v_lshl_add_u64 v[4:5], v[4:5], 0, v[2:3]
	global_load_dwordx2 v[6:7], v[4:5], off
	v_readlane_b32 s5, v252, 14
	v_readlane_b32 s1, v252, 11
	v_med3_u32 v15, v12, 8, 56
	v_add_u32_e32 v14, -8, v15
	v_lshlrev_b32_e32 v178, 4, v177
	s_mov_b32 s3, 0
	v_lshlrev_b32_e32 v189, 8, v176
	v_lshl_add_u32 v179, v176, 2, s89
	v_mov_b32_e32 v200, 0
	v_mov_b32_e32 v184, 0xf149f2ca
	s_waitcnt vmcnt(0)
	v_cvt_f32_fp8_e32 v0, v6
	v_cvt_f32_fp8_sdwa v8, v6 src0_sel:BYTE_1
	v_cvt_pk_bf16_f32 v0, v0, v8
	v_cvt_f32_fp8_sdwa v8, v6 src0_sel:BYTE_2
	v_cvt_f32_fp8_sdwa v6, v6 src0_sel:BYTE_3
	v_cvt_pk_bf16_f32 v8, v8, v6
	v_cvt_f32_fp8_e32 v6, v7
	v_cvt_f32_fp8_sdwa v9, v7 src0_sel:BYTE_1
	v_cvt_pk_bf16_f32 v9, v6, v9
	v_cvt_f32_fp8_sdwa v6, v7 src0_sel:BYTE_2
	v_cvt_f32_fp8_sdwa v7, v7 src0_sel:BYTE_3
	v_cvt_pk_bf16_f32 v10, v6, v7
	global_load_dwordx2 v[6:7], v[4:5], off offset:16
	v_and_b32_e32 v80, 0xffff0000, v0
	v_and_b32_e32 v78, 0xffff0000, v8
	v_lshlrev_b32_e32 v81, 16, v0
	v_lshlrev_b32_e32 v79, 16, v8
	v_mul_f32_e32 v0, v80, v80
	v_mul_f32_e32 v8, v78, v78
	v_and_b32_e32 v76, 0xffff0000, v9
	v_fmac_f32_e32 v0, v81, v81
	v_fmac_f32_e32 v8, v79, v79
	v_lshlrev_b32_e32 v77, 16, v9
	v_add_f32_e32 v0, v0, v8
	v_mul_f32_e32 v8, v76, v76
	v_and_b32_e32 v74, 0xffff0000, v10
	v_fmac_f32_e32 v8, v77, v77
	v_lshlrev_b32_e32 v75, 16, v10
	v_add_f32_e32 v0, v0, v8
	v_mul_f32_e32 v8, v74, v74
	v_fmac_f32_e32 v8, v75, v75
	v_add_f32_e32 v0, v0, v8
	s_waitcnt vmcnt(0)
	v_cvt_f32_fp8_e32 v11, v6
	v_cvt_f32_fp8_sdwa v17, v6 src0_sel:BYTE_1
	v_cvt_pk_bf16_f32 v11, v11, v17
	v_cvt_f32_fp8_sdwa v17, v6 src0_sel:BYTE_2
	v_cvt_f32_fp8_sdwa v6, v6 src0_sel:BYTE_3
	v_cvt_pk_bf16_f32 v18, v17, v6
	v_cvt_f32_fp8_e32 v6, v7
	v_cvt_f32_fp8_sdwa v17, v7 src0_sel:BYTE_1
	v_cvt_pk_bf16_f32 v19, v6, v17
	v_cvt_f32_fp8_sdwa v6, v7 src0_sel:BYTE_2
	v_cvt_f32_fp8_sdwa v7, v7 src0_sel:BYTE_3
	v_cvt_pk_bf16_f32 v20, v6, v7
	global_load_dwordx2 v[6:7], v[4:5], off offset:32
	v_and_b32_e32 v72, 0xffff0000, v11
	v_and_b32_e32 v70, 0xffff0000, v18
	v_lshlrev_b32_e32 v73, 16, v11
	v_lshlrev_b32_e32 v71, 16, v18
	v_mul_f32_e32 v8, v72, v72
	v_mul_f32_e32 v9, v70, v70
	v_and_b32_e32 v68, 0xffff0000, v19
	v_fmac_f32_e32 v8, v73, v73
	v_fmac_f32_e32 v9, v71, v71
	v_lshlrev_b32_e32 v69, 16, v19
	v_add_f32_e32 v8, v8, v9
	v_mul_f32_e32 v9, v68, v68
	v_and_b32_e32 v66, 0xffff0000, v20
	v_fmac_f32_e32 v9, v69, v69
	v_lshlrev_b32_e32 v67, 16, v20
	v_add_f32_e32 v8, v8, v9
	v_mul_f32_e32 v9, v66, v66
	v_fmac_f32_e32 v9, v67, v67
	v_add_f32_e32 v8, v8, v9
	v_add_f32_e32 v0, v0, v8
	s_waitcnt lgkmcnt(0)
	v_lshl_add_u64 v[10:11], v[2:3], 2, s[12:13]
	s_waitcnt vmcnt(0)
	v_cvt_f32_fp8_e32 v17, v6
	v_cvt_f32_fp8_sdwa v21, v6 src0_sel:BYTE_1
	v_cvt_pk_bf16_f32 v21, v17, v21
	v_cvt_f32_fp8_sdwa v17, v6 src0_sel:BYTE_2
	v_cvt_f32_fp8_sdwa v6, v6 src0_sel:BYTE_3
	v_cvt_pk_bf16_f32 v22, v17, v6
	v_cvt_f32_fp8_e32 v6, v7
	v_cvt_f32_fp8_sdwa v17, v7 src0_sel:BYTE_1
	v_cvt_pk_bf16_f32 v23, v6, v17
	v_cvt_f32_fp8_sdwa v6, v7 src0_sel:BYTE_2
	v_cvt_f32_fp8_sdwa v7, v7 src0_sel:BYTE_3
	v_cvt_pk_bf16_f32 v24, v6, v7
	global_load_dwordx2 v[6:7], v[4:5], off offset:48
	v_and_b32_e32 v64, 0xffff0000, v21
	v_and_b32_e32 v62, 0xffff0000, v22
	v_lshlrev_b32_e32 v65, 16, v21
	v_lshlrev_b32_e32 v63, 16, v22
	v_mul_f32_e32 v8, v64, v64
	v_mul_f32_e32 v9, v62, v62
	v_and_b32_e32 v60, 0xffff0000, v23
	v_fmac_f32_e32 v8, v65, v65
	v_fmac_f32_e32 v9, v63, v63
	v_lshlrev_b32_e32 v61, 16, v23
	v_add_f32_e32 v8, v8, v9
	v_mul_f32_e32 v9, v60, v60
	v_and_b32_e32 v58, 0xffff0000, v24
	v_fmac_f32_e32 v9, v61, v61
	v_lshlrev_b32_e32 v59, 16, v24
	v_add_f32_e32 v8, v8, v9
	v_mul_f32_e32 v9, v58, v58
	v_fmac_f32_e32 v9, v59, v59
	v_add_f32_e32 v8, v8, v9
	v_add_f32_e32 v0, v0, v8
	s_waitcnt vmcnt(0)
	v_cvt_f32_fp8_e32 v17, v6
	v_cvt_f32_fp8_sdwa v25, v6 src0_sel:BYTE_1
	v_cvt_pk_bf16_f32 v25, v17, v25
	v_cvt_f32_fp8_sdwa v17, v6 src0_sel:BYTE_2
	v_cvt_f32_fp8_sdwa v6, v6 src0_sel:BYTE_3
	v_cvt_pk_bf16_f32 v26, v17, v6
	v_cvt_f32_fp8_e32 v6, v7
	v_cvt_f32_fp8_sdwa v17, v7 src0_sel:BYTE_1
	v_cvt_pk_bf16_f32 v27, v6, v17
	v_cvt_f32_fp8_sdwa v6, v7 src0_sel:BYTE_2
	v_cvt_f32_fp8_sdwa v7, v7 src0_sel:BYTE_3
	v_cvt_pk_bf16_f32 v28, v6, v7
	global_load_dwordx2 v[6:7], v[4:5], off offset:64
	v_and_b32_e32 v56, 0xffff0000, v25
	v_and_b32_e32 v54, 0xffff0000, v26
	v_lshlrev_b32_e32 v57, 16, v25
	v_lshlrev_b32_e32 v55, 16, v26
	v_mul_f32_e32 v8, v56, v56
	v_mul_f32_e32 v9, v54, v54
	v_and_b32_e32 v52, 0xffff0000, v27
	v_fmac_f32_e32 v8, v57, v57
	v_fmac_f32_e32 v9, v55, v55
	v_lshlrev_b32_e32 v53, 16, v27
	v_add_f32_e32 v8, v8, v9
	v_mul_f32_e32 v9, v52, v52
	v_and_b32_e32 v50, 0xffff0000, v28
	v_fmac_f32_e32 v9, v53, v53
	v_lshlrev_b32_e32 v51, 16, v28
	v_add_f32_e32 v8, v8, v9
	v_mul_f32_e32 v9, v50, v50
	v_fmac_f32_e32 v9, v51, v51
	v_add_f32_e32 v8, v8, v9
	v_add_f32_e32 v0, v0, v8
	s_waitcnt vmcnt(0)
	v_cvt_f32_fp8_e32 v17, v6
	v_cvt_f32_fp8_sdwa v29, v6 src0_sel:BYTE_1
	v_cvt_pk_bf16_f32 v29, v17, v29
	v_cvt_f32_fp8_sdwa v17, v6 src0_sel:BYTE_2
	v_cvt_f32_fp8_sdwa v6, v6 src0_sel:BYTE_3
	v_cvt_pk_bf16_f32 v30, v17, v6
	v_cvt_f32_fp8_e32 v6, v7
	v_cvt_f32_fp8_sdwa v17, v7 src0_sel:BYTE_1
	v_cvt_pk_bf16_f32 v31, v6, v17
	v_cvt_f32_fp8_sdwa v6, v7 src0_sel:BYTE_2
	v_cvt_f32_fp8_sdwa v7, v7 src0_sel:BYTE_3
	v_cvt_pk_bf16_f32 v32, v6, v7
	global_load_dwordx2 v[6:7], v[4:5], off offset:80
	v_and_b32_e32 v48, 0xffff0000, v29
	v_and_b32_e32 v46, 0xffff0000, v30
	v_lshlrev_b32_e32 v49, 16, v29
	v_lshlrev_b32_e32 v47, 16, v30
	v_mul_f32_e32 v8, v48, v48
	v_mul_f32_e32 v9, v46, v46
	v_and_b32_e32 v44, 0xffff0000, v31
	v_fmac_f32_e32 v8, v49, v49
	v_fmac_f32_e32 v9, v47, v47
	v_lshlrev_b32_e32 v45, 16, v31
	v_add_f32_e32 v8, v8, v9
	v_mul_f32_e32 v9, v44, v44
	v_and_b32_e32 v42, 0xffff0000, v32
	v_fmac_f32_e32 v9, v45, v45
	v_lshlrev_b32_e32 v43, 16, v32
	v_add_f32_e32 v8, v8, v9
	v_mul_f32_e32 v9, v42, v42
	v_fmac_f32_e32 v9, v43, v43
	v_add_f32_e32 v8, v8, v9
	v_add_f32_e32 v0, v0, v8
	s_waitcnt vmcnt(0)
	v_cvt_f32_fp8_e32 v17, v6
	v_cvt_f32_fp8_sdwa v33, v6 src0_sel:BYTE_1
	v_cvt_pk_bf16_f32 v33, v17, v33
	v_cvt_f32_fp8_sdwa v17, v6 src0_sel:BYTE_2
	v_cvt_f32_fp8_sdwa v6, v6 src0_sel:BYTE_3
	v_cvt_pk_bf16_f32 v34, v17, v6
	v_cvt_f32_fp8_e32 v6, v7
	v_cvt_f32_fp8_sdwa v17, v7 src0_sel:BYTE_1
	v_cvt_pk_bf16_f32 v35, v6, v17
	v_cvt_f32_fp8_sdwa v6, v7 src0_sel:BYTE_2
	v_cvt_f32_fp8_sdwa v7, v7 src0_sel:BYTE_3
	v_cvt_pk_bf16_f32 v82, v6, v7
	global_load_dwordx2 v[6:7], v[4:5], off offset:96
	v_and_b32_e32 v40, 0xffff0000, v33
	v_and_b32_e32 v38, 0xffff0000, v34
	v_lshlrev_b32_e32 v41, 16, v33
	v_lshlrev_b32_e32 v39, 16, v34
	v_mul_f32_e32 v8, v40, v40
	v_mul_f32_e32 v9, v38, v38
	v_fmac_f32_e32 v8, v41, v41
	v_fmac_f32_e32 v9, v39, v39
	v_lshlrev_b32_e32 v37, 16, v35
	v_add_f32_e32 v8, v8, v9
	v_and_b32_e32 v34, 0xffff0000, v82
	s_waitcnt vmcnt(0)
	v_cvt_f32_fp8_e32 v17, v6
	v_cvt_f32_fp8_sdwa v36, v6 src0_sel:BYTE_1
	v_cvt_pk_bf16_f32 v83, v17, v36
	v_cvt_f32_fp8_sdwa v17, v6 src0_sel:BYTE_2
	v_cvt_f32_fp8_sdwa v6, v6 src0_sel:BYTE_3
	v_cvt_pk_bf16_f32 v6, v17, v6
	v_cvt_f32_fp8_e32 v17, v7
	v_cvt_f32_fp8_sdwa v36, v7 src0_sel:BYTE_1
	v_cvt_pk_bf16_f32 v84, v17, v36
	v_cvt_f32_fp8_sdwa v17, v7 src0_sel:BYTE_2
	v_cvt_f32_fp8_sdwa v7, v7 src0_sel:BYTE_3
	v_cvt_pk_bf16_f32 v7, v17, v7
	global_load_dwordx2 v[4:5], v[4:5], off offset:112
	v_and_b32_e32 v32, 0xffff0000, v83
	v_and_b32_e32 v30, 0xffff0000, v6
	v_lshlrev_b32_e32 v33, 16, v83
	v_lshlrev_b32_e32 v31, 16, v6
	v_lshlrev_b32_e32 v27, 16, v7
	v_and_b32_e32 v26, 0xffff0000, v7
	v_mul_f32_e32 v6, v32, v32
	v_mul_f32_e32 v7, v30, v30
	v_and_b32_e32 v28, 0xffff0000, v84
	v_fmac_f32_e32 v6, v33, v33
	v_fmac_f32_e32 v7, v31, v31
	v_lshlrev_b32_e32 v29, 16, v84
	v_add_f32_e32 v6, v6, v7
	v_mul_f32_e32 v7, v28, v28
	v_fmac_f32_e32 v7, v29, v29
	v_add_f32_e32 v6, v6, v7
	v_mul_f32_e32 v7, v26, v26
	v_fmac_f32_e32 v7, v27, v27
	v_add_f32_e32 v6, v6, v7
	s_waitcnt vmcnt(0)
	v_cvt_f32_fp8_e32 v17, v4
	v_cvt_f32_fp8_sdwa v36, v4 src0_sel:BYTE_1
	v_cvt_pk_bf16_f32 v85, v17, v36
	v_cvt_f32_fp8_sdwa v17, v4 src0_sel:BYTE_2
	v_cvt_f32_fp8_sdwa v4, v4 src0_sel:BYTE_3
	v_cvt_f32_fp8_sdwa v36, v5 src0_sel:BYTE_1
	v_cvt_pk_bf16_f32 v4, v17, v4
	v_cvt_f32_fp8_e32 v17, v5
	v_cvt_pk_bf16_f32 v86, v17, v36
	v_and_b32_e32 v36, 0xffff0000, v35
	v_mul_f32_e32 v9, v36, v36
	v_fmac_f32_e32 v9, v37, v37
	v_lshlrev_b32_e32 v35, 16, v82
	v_add_f32_e32 v8, v8, v9
	v_mul_f32_e32 v9, v34, v34
	v_fmac_f32_e32 v9, v35, v35
	v_cvt_f32_fp8_sdwa v17, v5 src0_sel:BYTE_2
	v_cvt_f32_fp8_sdwa v5, v5 src0_sel:BYTE_3
	v_add_f32_e32 v8, v8, v9
	v_cvt_pk_bf16_f32 v5, v17, v5
	v_add_f32_e32 v0, v0, v8
	v_and_b32_e32 v23, 0xffff0000, v85
	v_and_b32_e32 v21, 0xffff0000, v4
	v_add_f32_e32 v6, v0, v6
	v_lshlrev_b32_e32 v24, 16, v85
	v_lshlrev_b32_e32 v22, 16, v4
	v_lshlrev_b32_e32 v18, 16, v5
	v_and_b32_e32 v0, 0xffff0000, v5
	v_mul_f32_e32 v4, v23, v23
	v_mul_f32_e32 v5, v21, v21
	v_and_b32_e32 v19, 0xffff0000, v86
	v_fmac_f32_e32 v4, v24, v24
	v_fmac_f32_e32 v5, v22, v22
	v_lshlrev_b32_e32 v20, 16, v86
	v_add_f32_e32 v4, v4, v5
	v_mul_f32_e32 v5, v19, v19
	v_fmac_f32_e32 v5, v20, v20
	v_add_f32_e32 v4, v4, v5
	v_mul_f32_e32 v5, v0, v0
	v_fmac_f32_e32 v5, v18, v18
	v_add_f32_e32 v4, v4, v5
	v_add_f32_e32 v4, v6, v4
	v_mov_b32_e32 v5, v4
	s_nop 1
	v_permlane32_swap_b32_e32 v4, v5
	v_add_f32_e32 v4, v4, v5
	v_fmamk_f32 v4, v4, 0x3c000000, v167
	v_rsq_f32_e32 v25, v4
	s_nop 0
	v_add_u32_e32 v17, s1, v16
	s_movk_i32 s1, 0xffef
	global_load_dwordx4 v[2:5], v[10:11], off offset:16
	global_load_dwordx4 v[6:9], v[10:11], off
	v_mul_f32_e32 v81, v25, v81
	v_mul_f32_e32 v80, v25, v80
	v_mul_f32_e32 v73, v25, v73
	v_mul_f32_e32 v72, v25, v72
	v_mul_f32_e32 v65, v25, v65
	v_mul_f32_e32 v64, v25, v64
	v_mul_f32_e32 v57, v25, v57
	v_mul_f32_e32 v56, v25, v56
	v_mul_f32_e32 v49, v25, v49
	v_mul_f32_e32 v48, v25, v48
	v_mul_f32_e32 v41, v25, v41
	v_mul_f32_e32 v40, v25, v40
	v_mul_f32_e32 v33, v25, v33
	v_mul_f32_e32 v32, v25, v32
	v_mul_f32_e32 v0, v25, v0
	v_cmp_lt_i32_e32 vcc, v171, v172
	s_waitcnt vmcnt(0)
	v_mul_f32_e32 v6, v6, v81
	v_mul_f32_e32 v7, v7, v80
	v_cvt_pk_bf16_f32 v114, v6, v7
	v_mul_f32_e32 v6, v25, v79
	v_mul_f32_e32 v6, v8, v6
	v_mul_f32_e32 v7, v25, v78
	v_mul_f32_e32 v7, v9, v7
	v_cvt_pk_bf16_f32 v115, v6, v7
	v_mul_f32_e32 v6, v25, v77
	v_mul_f32_e32 v2, v2, v6
	v_mul_f32_e32 v6, v25, v76
	v_mul_f32_e32 v3, v3, v6
	v_cvt_pk_bf16_f32 v116, v2, v3
	v_mul_f32_e32 v2, v25, v75
	v_mul_f32_e32 v3, v25, v74
	v_mul_f32_e32 v2, v4, v2
	v_mul_f32_e32 v3, v5, v3
	v_cvt_pk_bf16_f32 v117, v2, v3
	global_load_dwordx4 v[2:5], v[10:11], off offset:80
	global_load_dwordx4 v[6:9], v[10:11], off offset:64
	s_waitcnt vmcnt(0)
	v_mul_f32_e32 v6, v6, v73
	v_mul_f32_e32 v7, v7, v72
	v_cvt_pk_bf16_f32 v118, v6, v7
	v_mul_f32_e32 v6, v25, v71
	v_mul_f32_e32 v6, v8, v6
	v_mul_f32_e32 v7, v25, v70
	v_mul_f32_e32 v7, v9, v7
	v_cvt_pk_bf16_f32 v119, v6, v7
	v_mul_f32_e32 v6, v25, v69
	v_mul_f32_e32 v2, v6, v2
	v_mul_f32_e32 v6, v25, v68
	v_mul_f32_e32 v3, v6, v3
	v_cvt_pk_bf16_f32 v120, v2, v3
	v_mul_f32_e32 v2, v25, v67
	v_mul_f32_e32 v3, v25, v66
	v_mul_f32_e32 v2, v2, v4
	v_mul_f32_e32 v3, v3, v5
	v_cvt_pk_bf16_f32 v121, v2, v3
	global_load_dwordx4 v[2:5], v[10:11], off offset:144
	global_load_dwordx4 v[6:9], v[10:11], off offset:128
	s_waitcnt vmcnt(0)
	v_mul_f32_e32 v6, v65, v6
	v_mul_f32_e32 v7, v64, v7
	v_cvt_pk_bf16_f32 v122, v6, v7
	v_mul_f32_e32 v6, v25, v63
	v_mul_f32_e32 v6, v6, v8
	v_mul_f32_e32 v7, v25, v62
	v_mul_f32_e32 v7, v7, v9
	v_cvt_pk_bf16_f32 v123, v6, v7
	v_mul_f32_e32 v6, v25, v61
	v_mul_f32_e32 v2, v6, v2
	v_mul_f32_e32 v6, v25, v60
	v_mul_f32_e32 v3, v6, v3
	v_cvt_pk_bf16_f32 v124, v2, v3
	v_mul_f32_e32 v2, v25, v59
	v_mul_f32_e32 v3, v25, v58
	v_mul_f32_e32 v2, v2, v4
	v_mul_f32_e32 v3, v3, v5
	v_cvt_pk_bf16_f32 v125, v2, v3
	global_load_dwordx4 v[2:5], v[10:11], off offset:208
	global_load_dwordx4 v[6:9], v[10:11], off offset:192
	s_waitcnt vmcnt(0)
	v_mul_f32_e32 v6, v57, v6
	v_mul_f32_e32 v7, v56, v7
	v_cvt_pk_bf16_f32 v126, v6, v7
	v_mul_f32_e32 v6, v25, v55
	v_mul_f32_e32 v6, v6, v8
	v_mul_f32_e32 v7, v25, v54
	v_mul_f32_e32 v7, v7, v9
	v_cvt_pk_bf16_f32 v127, v6, v7
	v_mul_f32_e32 v6, v25, v53
	v_mul_f32_e32 v2, v6, v2
	v_mul_f32_e32 v6, v25, v52
	v_mul_f32_e32 v3, v6, v3
	v_cvt_pk_bf16_f32 v128, v2, v3
	v_mul_f32_e32 v2, v25, v51
	v_mul_f32_e32 v3, v25, v50
	v_mul_f32_e32 v2, v2, v4
	v_mul_f32_e32 v3, v3, v5
	v_cvt_pk_bf16_f32 v129, v2, v3
	global_load_dwordx4 v[2:5], v[10:11], off offset:272
	global_load_dwordx4 v[6:9], v[10:11], off offset:256
	s_waitcnt vmcnt(0)
	v_mul_f32_e32 v6, v49, v6
	v_mul_f32_e32 v7, v48, v7
	v_cvt_pk_bf16_f32 v130, v6, v7
	v_mul_f32_e32 v6, v25, v47
	v_mul_f32_e32 v6, v6, v8
	v_mul_f32_e32 v7, v25, v46
	v_mul_f32_e32 v7, v7, v9
	v_cvt_pk_bf16_f32 v131, v6, v7
	v_mul_f32_e32 v6, v25, v45
	v_mul_f32_e32 v2, v6, v2
	v_mul_f32_e32 v6, v25, v44
	v_mul_f32_e32 v3, v6, v3
	v_cvt_pk_bf16_f32 v132, v2, v3
	v_mul_f32_e32 v2, v25, v43
	v_mul_f32_e32 v3, v25, v42
	v_mul_f32_e32 v2, v2, v4
	v_mul_f32_e32 v3, v3, v5
	v_cvt_pk_bf16_f32 v133, v2, v3
	global_load_dwordx4 v[2:5], v[10:11], off offset:336
	global_load_dwordx4 v[6:9], v[10:11], off offset:320
	s_waitcnt vmcnt(0)
	v_mul_f32_e32 v6, v41, v6
	v_mul_f32_e32 v7, v40, v7
	v_cvt_pk_bf16_f32 v134, v6, v7
	v_mul_f32_e32 v6, v25, v39
	v_mul_f32_e32 v6, v6, v8
	v_mul_f32_e32 v7, v25, v38
	v_mul_f32_e32 v7, v7, v9
	v_cvt_pk_bf16_f32 v135, v6, v7
	v_mul_f32_e32 v6, v25, v37
	v_mul_f32_e32 v2, v6, v2
	v_mul_f32_e32 v6, v25, v36
	v_mul_f32_e32 v3, v6, v3
	v_cvt_pk_bf16_f32 v136, v2, v3
	v_mul_f32_e32 v2, v25, v35
	v_mul_f32_e32 v3, v25, v34
	v_mul_f32_e32 v2, v2, v4
	v_mul_f32_e32 v3, v3, v5
	v_cvt_pk_bf16_f32 v137, v2, v3
	global_load_dwordx4 v[2:5], v[10:11], off offset:400
	global_load_dwordx4 v[6:9], v[10:11], off offset:384
	s_waitcnt vmcnt(0)
	v_mul_f32_e32 v6, v33, v6
	v_mul_f32_e32 v7, v32, v7
	v_cvt_pk_bf16_f32 v138, v6, v7
	v_mul_f32_e32 v6, v25, v31
	v_mul_f32_e32 v6, v6, v8
	v_mul_f32_e32 v7, v25, v30
	v_mul_f32_e32 v7, v7, v9
	v_cvt_pk_bf16_f32 v139, v6, v7
	v_mul_f32_e32 v6, v25, v29
	v_mul_f32_e32 v2, v6, v2
	v_mul_f32_e32 v6, v25, v28
	v_mul_f32_e32 v3, v6, v3
	v_cvt_pk_bf16_f32 v140, v2, v3
	v_mul_f32_e32 v2, v25, v27
	v_mul_f32_e32 v3, v25, v26
	v_mul_f32_e32 v2, v2, v4
	v_mul_f32_e32 v3, v3, v5
	v_cvt_pk_bf16_f32 v141, v2, v3
	global_load_dwordx4 v[2:5], v[10:11], off offset:464
	global_load_dwordx4 v[6:9], v[10:11], off offset:448
	v_mul_f32_e32 v10, v25, v24
	v_mov_b32_e32 v11, v1
	s_waitcnt vmcnt(1)
	v_mul_f32_e32 v0, v0, v5
	s_waitcnt vmcnt(0)
	v_mul_f32_e32 v6, v10, v6
	v_mul_f32_e32 v10, v25, v23
	v_mul_f32_e32 v7, v10, v7
	v_cvt_pk_bf16_f32 v142, v6, v7
	v_mul_f32_e32 v6, v25, v22
	v_mul_f32_e32 v6, v6, v8
	v_mul_f32_e32 v7, v25, v21
	v_mul_f32_e32 v7, v7, v9
	v_cvt_pk_bf16_f32 v143, v6, v7
	v_mul_f32_e32 v6, v25, v20
	v_mul_f32_e32 v2, v6, v2
	v_mul_f32_e32 v6, v25, v19
	v_mul_f32_e32 v3, v6, v3
	v_cvt_pk_bf16_f32 v144, v2, v3
	v_mul_f32_e32 v2, v25, v18
	v_ashrrev_i32_e32 v22, 4, v17
	v_mul_f32_e32 v2, v2, v4
	v_cvt_pk_bf16_f32 v145, v2, v0
	v_and_b32_e32 v0, 0xfffff0, v22
	v_lshlrev_b32_e32 v3, 1, v22
	v_lshlrev_b32_e32 v20, 3, v16
	v_and_or_b32 v0, v3, 8, v0
	v_and_b32_e32 v2, 0x78, v20
	v_lshrrev_b32_e32 v3, 1, v22
	v_lshrrev_b32_e32 v0, 1, v0
	v_bfe_u32 v4, v20, 5, 2
	v_and_b32_e32 v5, 3, v22
	v_or_b32_e32 v0, v0, v4
	v_and_or_b32 v3, v3, 4, v5
	v_lshlrev_b32_e32 v23, 1, v2
	v_lshlrev_b32_e32 v0, 9, v0
	v_lshlrev_b32_e32 v3, 6, v3
	v_and_b32_e32 v5, 48, v23
	v_add_u32_e32 v24, 32, v22
	v_or3_b32 v180, v0, v3, v5
	v_and_b32_e32 v0, 0xfffff0, v24
	v_lshlrev_b32_e32 v6, 1, v24
	v_and_or_b32 v0, v6, 8, v0
	v_lshrrev_b32_e32 v0, 1, v0
	v_or_b32_e32 v0, v0, v4
	v_lshlrev_b32_e32 v0, 9, v0
	v_or3_b32 v181, v0, v3, v5
	v_lshl_or_b32 v0, v22, 7, v2
	v_lshlrev_b32_e32 v2, 2, v2
	global_load_dwordx4 v[146:149], v2, s[10:11] offset:16
	global_load_dwordx4 v[150:153], v2, s[10:11]
	global_load_dwordx2 v[4:5], v0, s[8:9]
	v_add_u32_e32 v10, 0x1000, v0
	global_load_dwordx2 v[8:9], v10, s[8:9]
	global_load_dwordx2 v[26:27], v0, s[6:7]
	global_load_dwordx2 v[28:29], v10, s[6:7]
	s_waitcnt vmcnt(0)
	v_lshlrev_b32_e32 v21, 4, v16
	v_lshlrev_b32_e32 v19, 1, v16
	v_and_b32_e32 v18, 0xc0, v21
	v_bitop3_b32 v199, v21, v178, s33 bitop3:0x6c
	s_waitcnt vmcnt(3)
	v_cvt_f32_fp8_e32 v2, v4
	v_cvt_f32_fp8_sdwa v3, v4 src0_sel:BYTE_1
	v_cvt_pk_bf16_f32 v2, v2, v3
	v_cvt_f32_fp8_sdwa v3, v4 src0_sel:BYTE_2
	v_cvt_f32_fp8_sdwa v4, v4 src0_sel:BYTE_3
	v_cvt_pk_bf16_f32 v3, v3, v4
	v_cvt_f32_fp8_e32 v4, v5
	v_cvt_f32_fp8_sdwa v6, v5 src0_sel:BYTE_1
	v_cvt_pk_bf16_f32 v4, v4, v6
	v_cvt_f32_fp8_sdwa v6, v5 src0_sel:BYTE_2
	v_cvt_f32_fp8_sdwa v5, v5 src0_sel:BYTE_3
	v_cvt_pk_bf16_f32 v5, v6, v5
	s_waitcnt vmcnt(2)
	v_cvt_f32_fp8_e32 v6, v8
	v_cvt_f32_fp8_sdwa v7, v8 src0_sel:BYTE_1
	v_cvt_pk_bf16_f32 v6, v6, v7
	v_cvt_f32_fp8_sdwa v7, v8 src0_sel:BYTE_2
	v_cvt_f32_fp8_sdwa v8, v8 src0_sel:BYTE_3
	v_cvt_pk_bf16_f32 v7, v7, v8
	v_cvt_f32_fp8_e32 v8, v9
	v_cvt_f32_fp8_sdwa v25, v9 src0_sel:BYTE_1
	v_cvt_pk_bf16_f32 v8, v8, v25
	v_cvt_f32_fp8_sdwa v25, v9 src0_sel:BYTE_2
	v_cvt_f32_fp8_sdwa v9, v9 src0_sel:BYTE_3
	v_cvt_pk_bf16_f32 v9, v25, v9
	s_waitcnt vmcnt(1)
	v_cvt_f32_fp8_e32 v25, v26
	v_cvt_f32_fp8_sdwa v30, v26 src0_sel:BYTE_1
	v_cvt_pk_bf16_f32 v25, v25, v30
	v_cvt_f32_fp8_sdwa v30, v26 src0_sel:BYTE_2
	v_cvt_f32_fp8_sdwa v26, v26 src0_sel:BYTE_3
	v_cvt_pk_bf16_f32 v26, v30, v26
	v_cvt_f32_fp8_e32 v30, v27
	v_cvt_f32_fp8_sdwa v31, v27 src0_sel:BYTE_1
	v_cvt_pk_bf16_f32 v30, v30, v31
	v_cvt_f32_fp8_sdwa v31, v27 src0_sel:BYTE_2
	v_cvt_f32_fp8_sdwa v27, v27 src0_sel:BYTE_3
	v_cvt_pk_bf16_f32 v27, v31, v27
	s_waitcnt vmcnt(0)
	v_cvt_f32_fp8_e32 v31, v28
	v_cvt_f32_fp8_sdwa v32, v28 src0_sel:BYTE_1
	v_cvt_pk_bf16_f32 v31, v31, v32
	v_cvt_f32_fp8_sdwa v32, v28 src0_sel:BYTE_2
	v_cvt_f32_fp8_sdwa v28, v28 src0_sel:BYTE_3
	v_cvt_pk_bf16_f32 v32, v32, v28
	v_cvt_f32_fp8_e32 v28, v29
	v_cvt_f32_fp8_sdwa v33, v29 src0_sel:BYTE_1
	v_cvt_pk_bf16_f32 v33, v28, v33
	v_cvt_f32_fp8_sdwa v28, v29 src0_sel:BYTE_2
	v_cvt_f32_fp8_sdwa v29, v29 src0_sel:BYTE_3
	v_cvt_pk_bf16_f32 v34, v28, v29
	v_lshlrev_b32_e32 v28, 16, v25
	v_and_b32_e32 v25, 0xffff0000, v25
	v_and_b32_e32 v35, 0xffff0000, v26
	v_lshlrev_b32_e32 v29, 16, v26
	v_lshlrev_b32_e32 v37, 16, v27
	v_and_b32_e32 v38, 0xffff0000, v27
	v_mul_f32_e32 v26, v25, v25
	v_mul_f32_e32 v27, v35, v35
	v_lshlrev_b32_e32 v36, 16, v30
	v_and_b32_e32 v30, 0xffff0000, v30
	v_fmac_f32_e32 v26, v28, v28
	v_fmac_f32_e32 v27, v29, v29
	v_add_f32_e32 v26, v26, v27
	v_mul_f32_e32 v27, v30, v30
	v_fmac_f32_e32 v27, v36, v36
	v_add_f32_e32 v26, v26, v27
	v_mul_f32_e32 v27, v38, v38
	v_fmac_f32_e32 v27, v37, v37
	v_add_f32_e32 v26, v26, v27
	v_cndmask_b32_e32 v27, v170, v171, vcc
	v_lshlrev_b32_e32 v185, 2, v27
	ds_bpermute_b32 v27, v185, v26
	v_cmp_lt_i32_e32 vcc, v173, v172
	s_waitcnt lgkmcnt(0)
	v_add_f32_e32 v26, v26, v27
	v_cndmask_b32_e32 v27, v170, v173, vcc
	v_lshlrev_b32_e32 v186, 2, v27
	ds_bpermute_b32 v27, v186, v26
	v_cmp_lt_i32_e32 vcc, v174, v172
	s_waitcnt lgkmcnt(0)
	v_add_f32_e32 v26, v26, v27
	v_cndmask_b32_e32 v27, v170, v174, vcc
	v_lshlrev_b32_e32 v187, 2, v27
	ds_bpermute_b32 v27, v187, v26
	v_cmp_lt_i32_e32 vcc, v175, v172
	s_waitcnt lgkmcnt(0)
	v_add_f32_e32 v26, v26, v27
	v_cndmask_b32_e32 v27, v170, v175, vcc
	v_lshlrev_b32_e32 v188, 2, v27
	ds_bpermute_b32 v27, v188, v26
	s_waitcnt lgkmcnt(0)
	v_add_f32_e32 v26, v26, v27
	v_fmamk_f32 v26, v26, 0x3c000000, v167
	v_rsq_f32_e32 v39, v26
	s_nop 0
	v_mul_f32_e32 v26, v39, v28
	v_mul_f32_e32 v25, v39, v25
	v_mul_f32_e32 v26, v150, v26
	v_mul_f32_e32 v25, v151, v25
	v_cvt_pk_bf16_f32 v26, v26, v25
	v_mul_f32_e32 v25, v39, v29
	v_mul_f32_e32 v27, v39, v35
	v_mul_f32_e32 v25, v152, v25
	v_mul_f32_e32 v27, v153, v27
	v_cvt_pk_bf16_f32 v27, v25, v27
	v_mul_f32_e32 v25, v39, v36
	v_mul_f32_e32 v28, v39, v30
	v_mul_f32_e32 v25, v146, v25
	v_mul_f32_e32 v28, v147, v28
	v_cvt_pk_bf16_f32 v28, v25, v28
	v_mul_f32_e32 v25, v39, v37
	v_mul_f32_e32 v29, v39, v38
	v_mul_f32_e32 v25, v148, v25
	v_mul_f32_e32 v29, v149, v29
	v_cvt_pk_bf16_f32 v29, v25, v29
	v_lshlrev_b32_e32 v25, 16, v31
	v_and_b32_e32 v30, 0xffff0000, v31
	v_lshlrev_b32_e32 v31, 16, v32
	v_and_b32_e32 v32, 0xffff0000, v32
	v_mul_f32_e32 v37, v30, v30
	v_mul_f32_e32 v38, v32, v32
	v_lshlrev_b32_e32 v35, 16, v33
	v_and_b32_e32 v33, 0xffff0000, v33
	v_fmac_f32_e32 v37, v25, v25
	v_fmac_f32_e32 v38, v31, v31
	v_add_f32_e32 v37, v37, v38
	v_mul_f32_e32 v38, v33, v33
	v_lshlrev_b32_e32 v36, 16, v34
	v_and_b32_e32 v34, 0xffff0000, v34
	v_fmac_f32_e32 v38, v35, v35
	v_add_f32_e32 v37, v37, v38
	v_mul_f32_e32 v38, v34, v34
	v_fmac_f32_e32 v38, v36, v36
	v_add_f32_e32 v37, v37, v38
	ds_bpermute_b32 v38, v185, v37
	s_waitcnt lgkmcnt(0)
	v_add_f32_e32 v37, v37, v38
	ds_bpermute_b32 v38, v186, v37
	s_waitcnt lgkmcnt(0)
	v_add_f32_e32 v37, v37, v38
	ds_bpermute_b32 v38, v187, v37
	s_waitcnt lgkmcnt(0)
	v_add_f32_e32 v37, v37, v38
	ds_bpermute_b32 v38, v188, v37
	s_waitcnt lgkmcnt(0)
	v_add_f32_e32 v37, v37, v38
	v_fmamk_f32 v37, v37, 0x3c000000, v167
	v_rsq_f32_e32 v37, v37
	s_nop 0
	v_cmp_gt_u32_e64 s[4:5], 32, v16
	v_mul_f32_e32 v25, v37, v25
	v_mul_f32_e32 v30, v37, v30
	v_mul_f32_e32 v25, v150, v25
	v_mul_f32_e32 v30, v151, v30
	v_cvt_pk_bf16_f32 v30, v25, v30
	v_mul_f32_e32 v25, v37, v31
	v_mul_f32_e32 v31, v37, v32
	v_mul_f32_e32 v25, v152, v25
	v_mul_f32_e32 v31, v153, v31
	v_cvt_pk_bf16_f32 v31, v25, v31
	v_mul_f32_e32 v25, v37, v35
	v_mul_f32_e32 v32, v37, v33
	v_mul_f32_e32 v25, v146, v25
	v_mul_f32_e32 v32, v147, v32
	v_cvt_pk_bf16_f32 v32, v25, v32
	v_mul_f32_e32 v25, v37, v36
	v_mul_f32_e32 v33, v37, v34
	v_mul_f32_e32 v25, v148, v25
	v_mul_f32_e32 v33, v149, v33
	v_cvt_pk_bf16_f32 v33, v25, v33
	v_add_u32_e32 v25, 0, v180
	ds_write_b128 v25, v[2:5]
	v_add_u32_e32 v2, 0, v181
	ds_write_b128 v2, v[6:9]
	v_lshlrev_b32_e32 v2, 8, v22
	v_and_b32_e32 v3, 0xf0, v17
	v_bitop3_b32 v196, v23, v2, v3 bitop3:0xde
	v_add_u32_e32 v2, 0, v196
	ds_write_b128 v2, v[26:29] offset:32768
	v_lshlrev_b32_e32 v2, 8, v24
	v_bitop3_b32 v198, v2, v23, v3 bitop3:0xf6
	v_med3_i32 v3, s85, 4, v169
	v_add_u32_e32 v2, 0, v198
	v_readfirstlane_b32 s88, v3
	v_ashrrev_i32_e32 v3, 3, v13
	v_and_b32_e32 v4, -4, v3
	v_sub_u32_e32 v5, v4, v14
	v_cmp_gt_u32_e64 s[70:71], 16, v5
	v_sub_u32_e32 v5, v4, v15
	v_add_u32_e32 v6, 40, v5
	v_cmp_gt_u32_e64 s[68:69], 16, v6
	v_add_u32_e32 v6, 9, v5
	v_cmp_gt_u32_e64 s[66:67], 16, v6
	v_add_u32_e32 v6, 41, v5
	v_cmp_gt_u32_e64 s[64:65], 16, v6
	v_add_u32_e32 v6, 10, v5
	ds_write_b128 v2, v[30:33] offset:32768
	v_add_u32_e32 v2, 32, v178
	v_cmp_gt_u32_e64 s[62:63], 16, v6
	v_add_u32_e32 v6, 42, v5
	v_bitop3_b32 v197, v2, v21, s33 bitop3:0x78
	v_add_u32_e32 v2, 64, v178
	v_cmp_gt_u32_e64 s[60:61], 16, v6
	v_add_u32_e32 v6, 17, v5
	v_bitop3_b32 v195, v2, v21, s33 bitop3:0x78
	v_add_u32_e32 v2, 0x60, v178
	v_or_b32_e32 v3, 3, v3
	v_cmp_gt_u32_e64 s[50:51], 16, v6
	v_add_u32_e32 v6, 49, v5
	v_bitop3_b32 v194, v2, v21, s33 bitop3:0x78
	v_add_u32_e32 v2, 0x80, v178
	v_sub_u32_e32 v3, v3, v14
	v_cmp_gt_u32_e64 s[48:49], 16, v6
	v_add_u32_e32 v6, 18, v5
	v_bitop3_b32 v193, v2, v21, s33 bitop3:0x78
	v_add_u32_e32 v2, 0xa0, v178
	v_cmp_gt_u32_e64 s[58:59], 16, v3
	v_add_u32_e32 v3, 43, v5
	v_cmp_gt_u32_e64 s[46:47], 16, v6
	v_add_u32_e32 v6, 50, v5
	v_bitop3_b32 v192, v2, v21, s33 bitop3:0x78
	v_add_u32_e32 v2, 0xc0, v178
	v_cmp_gt_u32_e64 s[56:57], 16, v3
	v_cmp_lt_u32_e64 s[54:55], s1, v5
	v_and_b32_e32 v3, -16, v5
	s_movk_i32 s1, 0xffd0
	v_cmp_gt_u32_e64 s[44:45], 16, v6
	v_add_u32_e32 v6, 19, v5
	v_bitop3_b32 v191, v2, v21, s33 bitop3:0x78
	v_add_u32_e32 v2, 0xe0, v178
	s_add_i32 s84, s88, -4
	s_add_i32 s88, s88, 4
	v_cmp_eq_u32_e64 s[52:53], s1, v3
	v_cmp_gt_u32_e64 s[42:43], 16, v6
	v_add_u32_e32 v6, 51, v5
	s_movk_i32 s1, 0xffe0
	v_bitop3_b32 v190, v2, v21, s33 bitop3:0x78
	v_and_b32_e32 v2, 0x118, v20
	v_cmp_gt_u32_e64 s[40:41], 16, v6
	v_add_u32_e32 v6, 24, v5
	v_cmp_eq_u32_e64 s[20:21], s1, v3
	s_movk_i32 s1, 0xffc0
	s_cmp_lg_u32 0, -1
	v_and_or_b32 v2, v19, 32, v2
	v_cmp_gt_u32_e64 s[38:39], 16, v6
	v_add_u32_e32 v6, 56, v5
	v_cmp_eq_u32_e64 s[18:19], s1, v3
	s_cselect_b32 s1, 0, 0
	v_cmp_gt_u32_e64 s[36:37], 16, v6
	v_add_u32_e32 v6, 25, v5
	v_add_u32_e32 v3, 33, v5
	v_add3_u32 v182, v18, s1, v2
	v_readlane_b32 s1, v252, 25
	v_cmp_gt_u32_e64 s[34:35], 16, v6
	v_add_u32_e32 v6, 57, v5
	v_cmp_gt_u32_e64 s[16:17], 16, v3
	v_add_u32_e32 v3, 0x41, v5
	s_sub_i32 s2, s1, s86
	v_cmp_gt_u32_e64 s[30:31], 16, v6
	v_add_u32_e32 v6, 26, v5
	v_cmp_gt_u32_e64 s[14:15], 16, v3
	v_add_u32_e32 v3, 34, v5
	s_add_u32 s1, s78, s96
	v_cmp_gt_u32_e64 s[28:29], 16, v6
	v_add_u32_e32 v6, 58, v5
	v_cmp_gt_u32_e64 s[12:13], 16, v3
	v_add_u32_e32 v3, 0x42, v5
	s_addc_u32 s86, s79, s97
	v_cmp_gt_u32_e64 s[26:27], 16, v6
	v_add_u32_e32 v6, 27, v5
	v_cmp_gt_u32_e64 s[10:11], 16, v3
	v_add_u32_e32 v3, 35, v5
	s_add_u32 s72, s1, s72
	v_cmp_gt_u32_e64 s[24:25], 16, v6
	v_add_u32_e32 v6, 59, v5
	v_cmp_gt_u32_e64 s[8:9], 16, v3
	v_add_u32_e32 v3, 0x43, v5
	s_addc_u32 s73, s86, s73
	v_mov_b32_e32 v14, v1
	v_mov_b32_e32 v15, v1
	v_cmp_gt_u32_e64 s[22:23], 16, v6
	v_cmp_gt_u32_e64 s[6:7], 16, v3
	v_sub_u32_e32 v183, v4, v12
	v_lshl_add_u64 v[154:155], s[72:73], 0, v[0:1]
	v_lshl_add_u64 v[156:157], s[72:73], 0, v[10:11]
	v_mov_b32_e32 v0, v1
	v_mov_b32_e32 v2, v1
	v_mov_b32_e32 v3, v1
	v_mov_b32_e32 v4, v1
	v_mov_b32_e32 v5, v1
	v_mov_b32_e32 v6, v1
	v_mov_b32_e32 v7, v1
	v_mov_b32_e32 v8, v1
	v_mov_b32_e32 v9, v1
	v_mov_b32_e32 v10, v1
	v_mov_b32_e32 v12, v1
	v_mov_b32_e32 v13, v1
	v_mov_b64_e32 v[64:65], v[14:15]
	v_mov_b64_e32 v[48:49], v[14:15]
	v_mov_b64_e32 v[32:33], v[14:15]
	v_mov_b64_e32 v[62:63], v[12:13]
	v_mov_b64_e32 v[60:61], v[10:11]
	v_mov_b64_e32 v[58:59], v[8:9]
	v_mov_b64_e32 v[56:57], v[6:7]
	v_mov_b64_e32 v[54:55], v[4:5]
	v_mov_b64_e32 v[52:53], v[2:3]
	v_mov_b64_e32 v[50:51], v[0:1]
	v_mov_b64_e32 v[46:47], v[12:13]
	v_mov_b64_e32 v[44:45], v[10:11]
	v_mov_b64_e32 v[42:43], v[8:9]
	v_mov_b64_e32 v[40:41], v[6:7]
	v_mov_b64_e32 v[38:39], v[4:5]
	v_mov_b64_e32 v[36:37], v[2:3]
	v_mov_b64_e32 v[34:35], v[0:1]
	v_mov_b64_e32 v[30:31], v[12:13]
	v_mov_b64_e32 v[28:29], v[10:11]
	v_mov_b64_e32 v[26:27], v[8:9]
	v_mov_b64_e32 v[24:25], v[6:7]
	v_mov_b64_e32 v[22:23], v[4:5]
	v_mov_b64_e32 v[20:21], v[2:3]
	v_mov_b64_e32 v[18:19], v[0:1]
	v_mov_b64_e32 v[16:17], v[14:15]
	s_mov_b64 s[96:97], 0
	v_mov_b64_e32 v[14:15], v[12:13]
	v_mov_b64_e32 v[12:13], v[10:11]
	v_mov_b64_e32 v[10:11], v[8:9]
	v_mov_b64_e32 v[8:9], v[6:7]
	v_mov_b64_e32 v[6:7], v[4:5]
	v_mov_b64_e32 v[4:5], v[2:3]
	v_mov_b64_e32 v[2:3], v[0:1]
	s_waitcnt lgkmcnt(0)
	s_barrier

.LBB0_601:
	v_cndmask_b32_e64 v184, v98, v184, s[72:73]
	v_mul_f32_e32 v98, 0xbe0293ee, v184
	v_fmamk_f32 v82, v82, 0x3e0293ee, v98
	v_fmamk_f32 v83, v83, 0x3e0293ee, v98
	v_fmamk_f32 v84, v84, 0x3e0293ee, v98
	v_fmamk_f32 v85, v85, 0x3e0293ee, v98
	v_fmamk_f32 v86, v86, 0x3e0293ee, v98
	v_fmamk_f32 v87, v87, 0x3e0293ee, v98
	v_fmamk_f32 v88, v88, 0x3e0293ee, v98
	v_fmamk_f32 v89, v89, 0x3e0293ee, v98
	v_fmamk_f32 v90, v90, 0x3e0293ee, v98
	v_fmamk_f32 v91, v91, 0x3e0293ee, v98
	v_fmamk_f32 v92, v92, 0x3e0293ee, v98
	v_fmamk_f32 v93, v93, 0x3e0293ee, v98
	v_fmamk_f32 v94, v94, 0x3e0293ee, v98
	v_fmamk_f32 v95, v95, 0x3e0293ee, v98
	v_fmamk_f32 v96, v96, 0x3e0293ee, v98
	v_fmamk_f32 v97, v97, 0x3e0293ee, v98
	v_fmamk_f32 v0, v0, 0x3e0293ee, v98
	v_fmamk_f32 v66, v66, 0x3e0293ee, v98
	v_fmamk_f32 v67, v67, 0x3e0293ee, v98
	v_fmamk_f32 v68, v68, 0x3e0293ee, v98
	v_fmamk_f32 v69, v69, 0x3e0293ee, v98
	v_fmamk_f32 v70, v70, 0x3e0293ee, v98
	v_fmamk_f32 v71, v71, 0x3e0293ee, v98
	v_fmamk_f32 v72, v72, 0x3e0293ee, v98
	v_fmamk_f32 v73, v73, 0x3e0293ee, v98
	v_fmamk_f32 v74, v74, 0x3e0293ee, v98
	v_fmamk_f32 v75, v75, 0x3e0293ee, v98
	v_fmamk_f32 v76, v76, 0x3e0293ee, v98
	v_fmamk_f32 v77, v77, 0x3e0293ee, v98
	v_fmamk_f32 v78, v78, 0x3e0293ee, v98
	v_fmamk_f32 v79, v79, 0x3e0293ee, v98
	v_fmac_f32_e32 v98, 0x3e0293ee, v80
	v_exp_f32_e32 v80, v82
	v_exp_f32_e32 v82, v83
	v_exp_f32_e32 v83, v84
	v_exp_f32_e32 v84, v85
	v_exp_f32_e32 v85, v86
	v_exp_f32_e32 v86, v87
	v_exp_f32_e32 v87, v88
	v_exp_f32_e32 v88, v89
	v_exp_f32_e32 v89, v90
	v_exp_f32_e32 v90, v91
	v_exp_f32_e32 v91, v92
	v_exp_f32_e32 v92, v93
	v_exp_f32_e32 v93, v94
	v_exp_f32_e32 v94, v95
	v_exp_f32_e32 v95, v96
	v_exp_f32_e32 v96, v97
	v_exp_f32_e32 v97, v0
	v_add_f32_e32 v0, 0, v80
	v_add_f32_e32 v0, v82, v0
	v_add_f32_e32 v0, v83, v0
	v_add_f32_e32 v0, v84, v0
	v_add_f32_e32 v0, v85, v0
	v_add_f32_e32 v0, v86, v0
	v_add_f32_e32 v0, v87, v0
	v_add_f32_e32 v0, v88, v0
	v_add_f32_e32 v0, v89, v0
	v_add_f32_e32 v0, v90, v0
	v_add_f32_e32 v0, v91, v0
	v_add_f32_e32 v0, v92, v0
	v_add_f32_e32 v0, v93, v0
	v_exp_f32_e32 v99, v66
	v_add_f32_e32 v0, v94, v0
	v_exp_f32_e32 v100, v67
	v_add_f32_e32 v0, v95, v0
	v_exp_f32_e32 v101, v68
	v_add_f32_e32 v0, v96, v0
	v_exp_f32_e32 v102, v69
	v_add_f32_e32 v0, v97, v0
	v_exp_f32_e32 v103, v70
	v_add_f32_e32 v0, v99, v0
	v_exp_f32_e32 v104, v71
	v_add_f32_e32 v0, v100, v0
	v_exp_f32_e32 v105, v72
	v_add_f32_e32 v0, v101, v0
	v_exp_f32_e32 v106, v73
	v_add_f32_e32 v0, v102, v0
	v_exp_f32_e32 v107, v74
	v_add_f32_e32 v0, v103, v0
	v_exp_f32_e32 v108, v75
	v_add_f32_e32 v0, v104, v0
	v_exp_f32_e32 v109, v76
	v_add_f32_e32 v0, v105, v0
	v_exp_f32_e32 v110, v77
	v_add_f32_e32 v0, v106, v0
	v_exp_f32_e32 v111, v78
	v_add_f32_e32 v0, v107, v0
	v_exp_f32_e32 v112, v79
	v_add_f32_e32 v0, v108, v0
	v_exp_f32_e32 v98, v98
	v_add_f32_e32 v0, v109, v0
	v_add_f32_e32 v0, v110, v0
	v_add_f32_e32 v0, v111, v0
	v_add_f32_e32 v0, v112, v0
	v_add_f32_e32 v0, v98, v0
	v_mov_b32_e32 v66, v0
	s_nop 1
	v_permlane32_swap_b32_e32 v0, v66
	v_add_f32_e32 v0, v0, v66
	v_fmac_f32_e32 v0, v200, v81
	v_cvt_pk_bf16_f32 v66, v80, v82
	v_cvt_pk_bf16_f32 v67, v83, v84
	v_cvt_pk_bf16_f32 v68, v85, v86
	v_cvt_pk_bf16_f32 v69, v87, v88
	v_cvt_pk_bf16_f32 v70, v89, v90
	v_cvt_pk_bf16_f32 v71, v91, v92
	v_cvt_pk_bf16_f32 v72, v93, v94
	v_cvt_pk_bf16_f32 v73, v95, v96
	v_cvt_pk_bf16_f32 v74, v97, v99
	v_cvt_pk_bf16_f32 v75, v100, v101
	v_cvt_pk_bf16_f32 v76, v102, v103
	v_cvt_pk_bf16_f32 v77, v104, v105
	v_cvt_pk_bf16_f32 v78, v106, v107
	v_cvt_pk_bf16_f32 v79, v108, v109
	v_cvt_pk_bf16_f32 v80, v110, v111
	v_cvt_pk_bf16_f32 v81, v112, v98
	s_nop 0
	v_permlane32_swap_b32_e32 v66, v68
	v_permlane32_swap_b32_e32 v67, v69
	v_permlane32_swap_b32_e32 v70, v72
	v_permlane32_swap_b32_e32 v71, v73
	v_permlane32_swap_b32_e32 v74, v76
	v_permlane32_swap_b32_e32 v75, v77
	v_permlane32_swap_b32_e32 v78, v80
	v_permlane32_swap_b32_e32 v79, v81
	v_add_u32_e32 v98, s1, v182
	ds_read_b64_tr_b16 v[82:83], v98 offset:0
	ds_read_b64_tr_b16 v[84:85], v98 offset:0x800
	ds_read_b64_tr_b16 v[86:87], v98 offset:0x1000
	ds_read_b64_tr_b16 v[88:89], v98 offset:0x1800
	ds_read_b64_tr_b16 v[90:91], v98 offset:0x2000
	ds_read_b64_tr_b16 v[92:93], v98 offset:0x2800
	ds_read_b64_tr_b16 v[94:95], v98 offset:0x3000
	ds_read_b64_tr_b16 v[96:97], v98 offset:0x3800
	s_waitcnt lgkmcnt(0)
	s_nop 0
	v_mfma_f32_32x32x16_bf16 v[50:65], v[66:69], v[82:85], v[50:65]
	ds_read_b64_tr_b16 v[82:83], v98 offset:0x200
	ds_read_b64_tr_b16 v[84:85], v98 offset:0xa00
	v_mfma_f32_32x32x16_bf16 v[50:65], v[70:73], v[86:89], v[50:65]
	ds_read_b64_tr_b16 v[86:87], v98 offset:0x1200
	ds_read_b64_tr_b16 v[88:89], v98 offset:0x1a00
	v_mfma_f32_32x32x16_bf16 v[50:65], v[74:77], v[90:93], v[50:65]
	ds_read_b64_tr_b16 v[90:91], v98 offset:0x2200
	ds_read_b64_tr_b16 v[92:93], v98 offset:0x2a00
	v_mfma_f32_32x32x16_bf16 v[50:65], v[78:81], v[94:97], v[50:65]
	ds_read_b64_tr_b16 v[94:95], v98 offset:0x3200
	ds_read_b64_tr_b16 v[96:97], v98 offset:0x3a00
	s_waitcnt lgkmcnt(0)
	v_mfma_f32_32x32x16_bf16 v[34:49], v[66:69], v[82:85], v[34:49]
	ds_read_b64_tr_b16 v[82:83], v98 offset:0x400
	ds_read_b64_tr_b16 v[84:85], v98 offset:0xc00
	v_mfma_f32_32x32x16_bf16 v[34:49], v[70:73], v[86:89], v[34:49]
	ds_read_b64_tr_b16 v[86:87], v98 offset:0x1400
	ds_read_b64_tr_b16 v[88:89], v98 offset:0x1c00
	v_mfma_f32_32x32x16_bf16 v[34:49], v[74:77], v[90:93], v[34:49]
	ds_read_b64_tr_b16 v[90:91], v98 offset:0x2400
	ds_read_b64_tr_b16 v[92:93], v98 offset:0x2c00
	v_mfma_f32_32x32x16_bf16 v[34:49], v[78:81], v[94:97], v[34:49]
	ds_read_b64_tr_b16 v[94:95], v98 offset:0x3400
	ds_read_b64_tr_b16 v[96:97], v98 offset:0x3c00
	s_waitcnt lgkmcnt(0)
	v_mfma_f32_32x32x16_bf16 v[18:33], v[66:69], v[82:85], v[18:33]
	ds_read_b64_tr_b16 v[82:83], v98 offset:0x600
	ds_read_b64_tr_b16 v[84:85], v98 offset:0xe00
	v_mfma_f32_32x32x16_bf16 v[18:33], v[70:73], v[86:89], v[18:33]
	ds_read_b64_tr_b16 v[86:87], v98 offset:0x1600
	ds_read_b64_tr_b16 v[88:89], v98 offset:0x1e00
	v_mfma_f32_32x32x16_bf16 v[18:33], v[74:77], v[90:93], v[18:33]
	ds_read_b64_tr_b16 v[90:91], v98 offset:0x2600
	ds_read_b64_tr_b16 v[92:93], v98 offset:0x2e00
	v_mfma_f32_32x32x16_bf16 v[18:33], v[78:81], v[94:97], v[18:33]
	ds_read_b64_tr_b16 v[94:95], v98 offset:0x3600
	ds_read_b64_tr_b16 v[96:97], v98 offset:0x3e00
	s_waitcnt lgkmcnt(0)
	v_mfma_f32_32x32x16_bf16 v[2:17], v[66:69], v[82:85], v[2:17]
	s_waitcnt vmcnt(3)
	v_cvt_f32_fp8_e32 v66, v164
	v_cvt_f32_fp8_sdwa v67, v164 src0_sel:BYTE_1
	s_waitcnt vmcnt(0)
	v_cvt_pk_bf16_f32 v66, v66, v67
	v_cvt_f32_fp8_sdwa v67, v164 src0_sel:BYTE_2
	v_cvt_f32_fp8_sdwa v68, v164 src0_sel:BYTE_3
	v_cvt_pk_bf16_f32 v67, v67, v68
	v_mfma_f32_32x32x16_bf16 v[2:17], v[70:73], v[86:89], v[2:17]
	v_cvt_f32_fp8_e32 v68, v165
	v_cvt_f32_fp8_sdwa v69, v165 src0_sel:BYTE_1
	v_cvt_pk_bf16_f32 v68, v68, v69
	v_cvt_f32_fp8_sdwa v69, v165 src0_sel:BYTE_2
	v_cvt_f32_fp8_sdwa v70, v165 src0_sel:BYTE_3
	v_cvt_pk_bf16_f32 v69, v69, v70
	s_waitcnt vmcnt(2)
	v_cvt_f32_fp8_e32 v70, v162
	v_mfma_f32_32x32x16_bf16 v[2:17], v[74:77], v[90:93], v[2:17]
	v_cvt_f32_fp8_sdwa v71, v162 src0_sel:BYTE_1
	v_cvt_pk_bf16_f32 v70, v70, v71
	v_cvt_f32_fp8_sdwa v71, v162 src0_sel:BYTE_2
	v_cvt_f32_fp8_sdwa v72, v162 src0_sel:BYTE_3
	v_cvt_pk_bf16_f32 v71, v71, v72
	v_cvt_f32_fp8_e32 v72, v163
	v_cvt_f32_fp8_sdwa v73, v163 src0_sel:BYTE_1
	v_cvt_pk_bf16_f32 v72, v72, v73
	v_cvt_f32_fp8_sdwa v73, v163 src0_sel:BYTE_2
	v_cvt_f32_fp8_sdwa v74, v163 src0_sel:BYTE_3
	v_cvt_pk_bf16_f32 v73, v73, v74
	s_waitcnt vmcnt(1)
	v_cvt_f32_fp8_e32 v74, v160
	v_cvt_f32_fp8_sdwa v75, v160 src0_sel:BYTE_1
	v_cvt_pk_bf16_f32 v74, v74, v75
	v_cvt_f32_fp8_sdwa v75, v160 src0_sel:BYTE_2
	v_cvt_f32_fp8_sdwa v76, v160 src0_sel:BYTE_3
	v_cvt_pk_bf16_f32 v75, v75, v76
	v_cvt_f32_fp8_e32 v76, v161
	v_cvt_f32_fp8_sdwa v77, v161 src0_sel:BYTE_1
	v_mfma_f32_32x32x16_bf16 v[2:17], v[78:81], v[94:97], v[2:17]
	v_cvt_pk_bf16_f32 v76, v76, v77
	v_cvt_f32_fp8_sdwa v77, v161 src0_sel:BYTE_2
	v_cvt_f32_fp8_sdwa v78, v161 src0_sel:BYTE_3
	v_cvt_pk_bf16_f32 v77, v77, v78
	s_waitcnt vmcnt(0)
	v_cvt_f32_fp8_e32 v78, v158
	v_cvt_f32_fp8_sdwa v79, v158 src0_sel:BYTE_1
	v_cvt_pk_bf16_f32 v78, v78, v79
	v_cvt_f32_fp8_sdwa v79, v158 src0_sel:BYTE_2
	v_cvt_f32_fp8_sdwa v80, v158 src0_sel:BYTE_3
	v_cvt_pk_bf16_f32 v79, v79, v80
	v_cvt_f32_fp8_e32 v80, v159
	v_cvt_f32_fp8_sdwa v81, v159 src0_sel:BYTE_1
	v_cvt_pk_bf16_f32 v80, v80, v81
	v_cvt_f32_fp8_sdwa v81, v159 src0_sel:BYTE_2
	v_cvt_f32_fp8_sdwa v82, v159 src0_sel:BYTE_3
	v_cvt_pk_bf16_f32 v81, v81, v82
	v_lshlrev_b32_e32 v82, 16, v74
	v_and_b32_e32 v74, 0xffff0000, v74
	v_lshlrev_b32_e32 v83, 16, v75
	v_and_b32_e32 v75, 0xffff0000, v75
	v_mul_f32_e32 v86, v74, v74
	v_mul_f32_e32 v87, v75, v75
	v_lshlrev_b32_e32 v84, 16, v76
	v_and_b32_e32 v76, 0xffff0000, v76
	v_fmac_f32_e32 v86, v82, v82
	v_fmac_f32_e32 v87, v83, v83
	v_add_f32_e32 v86, v86, v87
	v_mul_f32_e32 v87, v76, v76
	v_lshlrev_b32_e32 v85, 16, v77
	v_and_b32_e32 v77, 0xffff0000, v77
	v_fmac_f32_e32 v87, v84, v84
	v_add_f32_e32 v86, v86, v87
	v_mul_f32_e32 v87, v77, v77
	v_fmac_f32_e32 v87, v85, v85
	v_add_f32_e32 v86, v86, v87
	ds_bpermute_b32 v87, v185, v86
	s_xor_b32 s1, s1, 0x4000
	s_add_i32 s1, s1, 0
	s_add_i32 s92, s92, 1
	s_addk_i32 s3, 0x4000
	s_waitcnt lgkmcnt(0)
	v_add_f32_e32 v86, v86, v87
	ds_bpermute_b32 v87, v186, v86
	s_add_u32 s96, s96, 0x2000
	s_addc_u32 s97, s97, 0
	s_cmp_eq_u32 s96, 0x16000
	s_waitcnt lgkmcnt(0)
	v_add_f32_e32 v86, v86, v87
	ds_bpermute_b32 v87, v187, v86
	s_waitcnt lgkmcnt(0)
	v_add_f32_e32 v86, v86, v87
	ds_bpermute_b32 v87, v188, v86
	s_waitcnt lgkmcnt(0)
	v_add_f32_e32 v86, v86, v87
	v_fmamk_f32 v86, v86, 0x3c000000, v167
	v_rsq_f32_e32 v86, v86
	s_nop 0
	v_mul_f32_e32 v82, v86, v82
	v_mul_f32_e32 v74, v86, v74
	v_mul_f32_e32 v82, v150, v82
	v_mul_f32_e32 v74, v151, v74
	v_cvt_pk_bf16_f32 v74, v82, v74
	v_mul_f32_e32 v82, v86, v83
	v_mul_f32_e32 v75, v86, v75
	v_mul_f32_e32 v82, v152, v82
	v_mul_f32_e32 v75, v153, v75
	v_cvt_pk_bf16_f32 v75, v82, v75
	v_mul_f32_e32 v82, v86, v84
	v_mul_f32_e32 v76, v86, v76
	v_mul_f32_e32 v82, v146, v82
	v_mul_f32_e32 v76, v147, v76
	v_cvt_pk_bf16_f32 v76, v82, v76
	v_mul_f32_e32 v82, v86, v85
	v_mul_f32_e32 v77, v86, v77
	v_mul_f32_e32 v82, v148, v82
	v_mul_f32_e32 v77, v149, v77
	v_cvt_pk_bf16_f32 v77, v82, v77
	v_lshlrev_b32_e32 v82, 16, v78
	v_and_b32_e32 v78, 0xffff0000, v78
	v_lshlrev_b32_e32 v83, 16, v79
	v_and_b32_e32 v79, 0xffff0000, v79
	v_mul_f32_e32 v86, v78, v78
	v_mul_f32_e32 v87, v79, v79
	v_lshlrev_b32_e32 v84, 16, v80
	v_and_b32_e32 v80, 0xffff0000, v80
	v_fmac_f32_e32 v86, v82, v82
	v_fmac_f32_e32 v87, v83, v83
	v_add_f32_e32 v86, v86, v87
	v_mul_f32_e32 v87, v80, v80
	v_lshlrev_b32_e32 v85, 16, v81
	v_and_b32_e32 v81, 0xffff0000, v81
	v_fmac_f32_e32 v87, v84, v84
	v_add_f32_e32 v86, v86, v87
	v_mul_f32_e32 v87, v81, v81
	v_fmac_f32_e32 v87, v85, v85
	v_add_f32_e32 v86, v86, v87
	ds_bpermute_b32 v87, v185, v86
	s_waitcnt lgkmcnt(0)
	v_add_f32_e32 v86, v86, v87
	ds_bpermute_b32 v87, v186, v86
	s_waitcnt lgkmcnt(0)
	v_add_f32_e32 v86, v86, v87
	ds_bpermute_b32 v87, v187, v86
	s_waitcnt lgkmcnt(0)
	v_add_f32_e32 v86, v86, v87
	ds_bpermute_b32 v87, v188, v86
	s_waitcnt lgkmcnt(0)
	v_add_f32_e32 v86, v86, v87
	v_fmamk_f32 v86, v86, 0x3c000000, v167
	v_rsq_f32_e32 v86, v86
	s_nop 0
	v_mul_f32_e32 v82, v86, v82
	v_mul_f32_e32 v78, v86, v78
	v_mul_f32_e32 v82, v150, v82
	v_mul_f32_e32 v78, v151, v78
	v_cvt_pk_bf16_f32 v78, v82, v78
	v_mul_f32_e32 v82, v86, v83
	v_mul_f32_e32 v79, v86, v79
	v_mul_f32_e32 v82, v152, v82
	v_mul_f32_e32 v79, v153, v79
	v_cvt_pk_bf16_f32 v79, v82, v79
	v_mul_f32_e32 v82, v86, v84
	v_mul_f32_e32 v80, v86, v80
	v_mul_f32_e32 v82, v146, v82
	v_mul_f32_e32 v80, v147, v80
	v_cvt_pk_bf16_f32 v80, v82, v80
	v_mul_f32_e32 v82, v86, v85
	v_mul_f32_e32 v81, v86, v81
	v_mul_f32_e32 v82, v148, v82
	v_mul_f32_e32 v81, v149, v81
	v_cvt_pk_bf16_f32 v81, v82, v81
	v_add_u32_e32 v82, s1, v180
	ds_write_b128 v82, v[66:69]
	v_add_u32_e32 v66, s1, v181
	ds_write_b128 v66, v[70:73]
	v_add_u32_e32 v66, s1, v196
	ds_write_b128 v66, v[74:77] offset:32768
	v_add_u32_e32 v66, s1, v198
	ds_write_b128 v66, v[78:81] offset:32768
	s_waitcnt lgkmcnt(0)
	s_barrier
	s_cbranch_scc1 .LBB0_603
	v_mov_b32_e32 v200, v0
	s_branch .LBB0_469
.Lna_skip:
	s_waitcnt vmcnt(3)
	v_cvt_f32_fp8_e32 v66, v164
	v_cvt_f32_fp8_sdwa v67, v164 src0_sel:BYTE_1
	s_waitcnt vmcnt(0)
	v_cvt_pk_bf16_f32 v66, v66, v67
	v_cvt_f32_fp8_sdwa v67, v164 src0_sel:BYTE_2
	v_cvt_f32_fp8_sdwa v68, v164 src0_sel:BYTE_3
	v_cvt_pk_bf16_f32 v67, v67, v68
	v_cvt_f32_fp8_e32 v68, v165
	v_cvt_f32_fp8_sdwa v69, v165 src0_sel:BYTE_1
	v_cvt_pk_bf16_f32 v68, v68, v69
	v_cvt_f32_fp8_sdwa v69, v165 src0_sel:BYTE_2
	v_cvt_f32_fp8_sdwa v70, v165 src0_sel:BYTE_3
	v_cvt_pk_bf16_f32 v69, v69, v70
	s_waitcnt vmcnt(2)
	v_cvt_f32_fp8_e32 v70, v162
	v_cvt_f32_fp8_sdwa v71, v162 src0_sel:BYTE_1
	v_cvt_pk_bf16_f32 v70, v70, v71
	v_cvt_f32_fp8_sdwa v71, v162 src0_sel:BYTE_2
	v_cvt_f32_fp8_sdwa v72, v162 src0_sel:BYTE_3
	v_cvt_pk_bf16_f32 v71, v71, v72
	v_cvt_f32_fp8_e32 v72, v163
	v_cvt_f32_fp8_sdwa v73, v163 src0_sel:BYTE_1
	v_cvt_pk_bf16_f32 v72, v72, v73
	v_cvt_f32_fp8_sdwa v73, v163 src0_sel:BYTE_2
	v_cvt_f32_fp8_sdwa v74, v163 src0_sel:BYTE_3
	v_cvt_pk_bf16_f32 v73, v73, v74
	s_waitcnt vmcnt(1)
	v_cvt_f32_fp8_e32 v74, v160
	v_cvt_f32_fp8_sdwa v75, v160 src0_sel:BYTE_1
	v_cvt_pk_bf16_f32 v74, v74, v75
	v_cvt_f32_fp8_sdwa v75, v160 src0_sel:BYTE_2
	v_cvt_f32_fp8_sdwa v76, v160 src0_sel:BYTE_3
	v_cvt_pk_bf16_f32 v75, v75, v76
	v_cvt_f32_fp8_e32 v76, v161
	v_cvt_f32_fp8_sdwa v77, v161 src0_sel:BYTE_1
	v_cvt_pk_bf16_f32 v76, v76, v77
	v_cvt_f32_fp8_sdwa v77, v161 src0_sel:BYTE_2
	v_cvt_f32_fp8_sdwa v78, v161 src0_sel:BYTE_3
	v_cvt_pk_bf16_f32 v77, v77, v78
	s_waitcnt vmcnt(0)
	v_cvt_f32_fp8_e32 v78, v158
	v_cvt_f32_fp8_sdwa v79, v158 src0_sel:BYTE_1
	v_cvt_pk_bf16_f32 v78, v78, v79
	v_cvt_f32_fp8_sdwa v79, v158 src0_sel:BYTE_2
	v_cvt_f32_fp8_sdwa v80, v158 src0_sel:BYTE_3
	v_cvt_pk_bf16_f32 v79, v79, v80
	v_cvt_f32_fp8_e32 v80, v159
	v_cvt_f32_fp8_sdwa v81, v159 src0_sel:BYTE_1
	v_cvt_pk_bf16_f32 v80, v80, v81
	v_cvt_f32_fp8_sdwa v81, v159 src0_sel:BYTE_2
	v_cvt_f32_fp8_sdwa v82, v159 src0_sel:BYTE_3
	v_cvt_pk_bf16_f32 v81, v81, v82
	v_lshlrev_b32_e32 v82, 16, v74
	v_and_b32_e32 v74, 0xffff0000, v74
	v_lshlrev_b32_e32 v83, 16, v75
	v_and_b32_e32 v75, 0xffff0000, v75
	v_mul_f32_e32 v86, v74, v74
	v_mul_f32_e32 v87, v75, v75
	v_lshlrev_b32_e32 v84, 16, v76
	v_and_b32_e32 v76, 0xffff0000, v76
	v_fmac_f32_e32 v86, v82, v82
	v_fmac_f32_e32 v87, v83, v83
	v_add_f32_e32 v86, v86, v87
	v_mul_f32_e32 v87, v76, v76
	v_lshlrev_b32_e32 v85, 16, v77
	v_and_b32_e32 v77, 0xffff0000, v77
	v_fmac_f32_e32 v87, v84, v84
	v_add_f32_e32 v86, v86, v87
	v_mul_f32_e32 v87, v77, v77
	v_fmac_f32_e32 v87, v85, v85
	v_add_f32_e32 v86, v86, v87
	ds_bpermute_b32 v87, v185, v86
	s_xor_b32 s1, s1, 0x4000
	s_add_i32 s1, s1, 0
	s_add_i32 s92, s92, 1
	s_addk_i32 s3, 0x4000
	s_waitcnt lgkmcnt(0)
	v_add_f32_e32 v86, v86, v87
	ds_bpermute_b32 v87, v186, v86
	s_add_u32 s96, s96, 0x2000
	s_addc_u32 s97, s97, 0
	s_cmp_eq_u32 s96, 0x16000
	s_waitcnt lgkmcnt(0)
	v_add_f32_e32 v86, v86, v87
	ds_bpermute_b32 v87, v187, v86
	s_waitcnt lgkmcnt(0)
	v_add_f32_e32 v86, v86, v87
	ds_bpermute_b32 v87, v188, v86
	s_waitcnt lgkmcnt(0)
	v_add_f32_e32 v86, v86, v87
	v_fmamk_f32 v86, v86, 0x3c000000, v167
	v_rsq_f32_e32 v86, v86
	s_nop 0
	v_mul_f32_e32 v82, v86, v82
	v_mul_f32_e32 v74, v86, v74
	v_mul_f32_e32 v82, v150, v82
	v_mul_f32_e32 v74, v151, v74
	v_cvt_pk_bf16_f32 v74, v82, v74
	v_mul_f32_e32 v82, v86, v83
	v_mul_f32_e32 v75, v86, v75
	v_mul_f32_e32 v82, v152, v82
	v_mul_f32_e32 v75, v153, v75
	v_cvt_pk_bf16_f32 v75, v82, v75
	v_mul_f32_e32 v82, v86, v84
	v_mul_f32_e32 v76, v86, v76
	v_mul_f32_e32 v82, v146, v82
	v_mul_f32_e32 v76, v147, v76
	v_cvt_pk_bf16_f32 v76, v82, v76
	v_mul_f32_e32 v82, v86, v85
	v_mul_f32_e32 v77, v86, v77
	v_mul_f32_e32 v82, v148, v82
	v_mul_f32_e32 v77, v149, v77
	v_cvt_pk_bf16_f32 v77, v82, v77
	v_lshlrev_b32_e32 v82, 16, v78
	v_and_b32_e32 v78, 0xffff0000, v78
	v_lshlrev_b32_e32 v83, 16, v79
	v_and_b32_e32 v79, 0xffff0000, v79
	v_mul_f32_e32 v86, v78, v78
	v_mul_f32_e32 v87, v79, v79
	v_lshlrev_b32_e32 v84, 16, v80
	v_and_b32_e32 v80, 0xffff0000, v80
	v_fmac_f32_e32 v86, v82, v82
	v_fmac_f32_e32 v87, v83, v83
	v_add_f32_e32 v86, v86, v87
	v_mul_f32_e32 v87, v80, v80
	v_lshlrev_b32_e32 v85, 16, v81
	v_and_b32_e32 v81, 0xffff0000, v81
	v_fmac_f32_e32 v87, v84, v84
	v_add_f32_e32 v86, v86, v87
	v_mul_f32_e32 v87, v81, v81
	v_fmac_f32_e32 v87, v85, v85
	v_add_f32_e32 v86, v86, v87
	ds_bpermute_b32 v87, v185, v86
	s_waitcnt lgkmcnt(0)
	v_add_f32_e32 v86, v86, v87
	ds_bpermute_b32 v87, v186, v86
	s_waitcnt lgkmcnt(0)
	v_add_f32_e32 v86, v86, v87
	ds_bpermute_b32 v87, v187, v86
	s_waitcnt lgkmcnt(0)
	v_add_f32_e32 v86, v86, v87
	ds_bpermute_b32 v87, v188, v86
	s_waitcnt lgkmcnt(0)
	v_add_f32_e32 v86, v86, v87
	v_fmamk_f32 v86, v86, 0x3c000000, v167
	v_rsq_f32_e32 v86, v86
	s_nop 0
	v_mul_f32_e32 v82, v86, v82
	v_mul_f32_e32 v78, v86, v78
	v_mul_f32_e32 v82, v150, v82
	v_mul_f32_e32 v78, v151, v78
	v_cvt_pk_bf16_f32 v78, v82, v78
	v_mul_f32_e32 v82, v86, v83
	v_mul_f32_e32 v79, v86, v79
	v_mul_f32_e32 v82, v152, v82
	v_mul_f32_e32 v79, v153, v79
	v_cvt_pk_bf16_f32 v79, v82, v79
	v_mul_f32_e32 v82, v86, v84
	v_mul_f32_e32 v80, v86, v80
	v_mul_f32_e32 v82, v146, v82
	v_mul_f32_e32 v80, v147, v80
	v_cvt_pk_bf16_f32 v80, v82, v80
	v_mul_f32_e32 v82, v86, v85
	v_mul_f32_e32 v81, v86, v81
	v_mul_f32_e32 v82, v148, v82
	v_mul_f32_e32 v81, v149, v81
	v_cvt_pk_bf16_f32 v81, v82, v81
	v_add_u32_e32 v82, s1, v180
	ds_write_b128 v82, v[66:69]
	v_add_u32_e32 v66, s1, v181
	ds_write_b128 v66, v[70:73]
	v_add_u32_e32 v66, s1, v196
	ds_write_b128 v66, v[74:77] offset:32768
	v_add_u32_e32 v66, s1, v198
	ds_write_b128 v66, v[78:81] offset:32768
	v_mov_b32_e32 v0, v200
	s_waitcnt lgkmcnt(0)
	s_barrier
	s_cbranch_scc1 .LBB0_603
	s_branch .LBB0_469
